# GEMM full-tile K loops: first iteration peeled with zero C operand, per-unit accumulator clears removed
# speedup vs baseline: 1.0122x; 1.0122x over previous
.LBB0_260:
	s_mov_b32 s18, s24
	s_mov_b32 s16, s19
	s_ashr_i32 s19, s24, 31
	s_lshl_b64 s[22:23], s[18:19], 19
	s_add_u32 s22, s33, s22
	s_addc_u32 s23, s40, s23
	s_and_b64 s[24:25], s[20:21], exec
	s_cselect_b32 s19, s23, s31
	s_cselect_b32 s27, s22, s30
	s_ashr_i32 s17, s16, 31
	s_lshl_b64 s[24:25], s[16:17], 19
	s_add_u32 s24, s41, s24
	s_addc_u32 s25, s42, s25
	s_and_b64 s[38:39], s[20:21], exec
	s_cselect_b32 s17, s25, s35
	s_cselect_b32 s58, s24, s34
	s_add_u32 s30, s30, 0x40080
	s_addc_u32 s31, s31, 0
	s_add_u32 s59, s34, 0x100
	s_addc_u32 s60, s35, 0
	s_mov_b32 s61, -2
	ds_read_b128 v[150:153], v144
	ds_read_b128 v[154:157], v144 offset:1024
	ds_read_b128 v[158:161], v144 offset:2048
	ds_read_b128 v[162:165], v144 offset:3072
	ds_read_b128 v[166:169], v145
	ds_read_b128 v[170:173], v145 offset:1024
	ds_read_b128 v[174:177], v145 offset:2048
	ds_read_b128 v[178:181], v145 offset:3072
	s_add_u32 s34, s30, 0xfffc0080
	s_addc_u32 s35, s31, -1
	s_cmp_eq_u32 s61, 12
	s_cselect_b32 s39, s19, s35
	s_cselect_b32 s38, s27, s34
	s_cselect_b32 s35, s17, s60
	s_cselect_b32 s34, s58, s59
	v_lshl_add_u64 v[142:143], s[30:31], 0, v[138:139]
	s_add_i32 m0, s29, 0xc000
	ds_read_b128 v[182:185], v146
	ds_read_b128 v[186:189], v146 offset:1024
	ds_read_b128 v[190:193], v146 offset:2048
	ds_read_b128 v[194:197], v146 offset:3072
	ds_read_b128 v[198:201], v146 offset:4096
	ds_read_b128 v[202:205], v146 offset:5120
	ds_read_b128 v[206:209], v146 offset:6144
	ds_read_b128 v[210:213], v146 offset:7168
	global_load_lds_dwordx4 v[142:143], off
	v_lshl_add_u64 v[142:143], s[30:31], 0, v[140:141]
	s_add_i32 m0, s29, 0xe000
	s_nop 0
	global_load_lds_dwordx4 v[142:143], off
	s_waitcnt vmcnt(8)
	s_waitcnt lgkmcnt(0)
	s_barrier
	s_setprio 1
	s_waitcnt lgkmcnt(0)
	v_mfma_i32_16x16x64_i8 v[126:129], v[150:153], v[182:185], 0
	v_mfma_i32_16x16x64_i8 v[122:125], v[158:161], v[182:185], 0
	v_mfma_i32_16x16x64_i8 v[110:113], v[150:153], v[190:193], 0
	v_mfma_i32_16x16x64_i8 v[106:109], v[158:161], v[190:193], 0
	v_mfma_i32_16x16x64_i8 v[98:101], v[150:153], v[198:201], 0
	v_mfma_i32_16x16x64_i8 v[90:93], v[158:161], v[198:201], 0
	v_mfma_i32_16x16x64_i8 v[82:85], v[150:153], v[206:209], 0
	v_mfma_i32_16x16x64_i8 v[74:77], v[158:161], v[206:209], 0
	v_mfma_i32_16x16x64_i8 v[126:129], v[154:157], v[186:189], v[126:129]
	v_mfma_i32_16x16x64_i8 v[122:125], v[162:165], v[186:189], v[122:125]
	v_mfma_i32_16x16x64_i8 v[110:113], v[154:157], v[194:197], v[110:113]
	v_mfma_i32_16x16x64_i8 v[106:109], v[162:165], v[194:197], v[106:109]
	v_mfma_i32_16x16x64_i8 v[98:101], v[154:157], v[202:205], v[98:101]
	v_mfma_i32_16x16x64_i8 v[90:93], v[162:165], v[202:205], v[90:93]
	v_mfma_i32_16x16x64_i8 v[82:85], v[154:157], v[210:213], v[82:85]
	v_mfma_i32_16x16x64_i8 v[74:77], v[162:165], v[210:213], v[74:77]
	s_setprio 0
	s_setprio 1
	v_mfma_i32_16x16x64_i8 v[118:121], v[166:169], v[182:185], 0
	v_mfma_i32_16x16x64_i8 v[114:117], v[174:177], v[182:185], 0
	v_mfma_i32_16x16x64_i8 v[102:105], v[166:169], v[190:193], 0
	v_mfma_i32_16x16x64_i8 v[94:97], v[174:177], v[190:193], 0
	v_mfma_i32_16x16x64_i8 v[86:89], v[166:169], v[198:201], 0
	v_mfma_i32_16x16x64_i8 v[78:81], v[174:177], v[198:201], 0
	v_mfma_i32_16x16x64_i8 v[70:73], v[166:169], v[206:209], 0
	v_mfma_i32_16x16x64_i8 v[66:69], v[174:177], v[206:209], 0
	v_mfma_i32_16x16x64_i8 v[118:121], v[170:173], v[186:189], v[118:121]
	v_mfma_i32_16x16x64_i8 v[114:117], v[178:181], v[186:189], v[114:117]
	v_mfma_i32_16x16x64_i8 v[102:105], v[170:173], v[194:197], v[102:105]
	v_mfma_i32_16x16x64_i8 v[94:97], v[178:181], v[194:197], v[94:97]
	v_mfma_i32_16x16x64_i8 v[86:89], v[170:173], v[202:205], v[86:89]
	v_mfma_i32_16x16x64_i8 v[78:81], v[178:181], v[202:205], v[78:81]
	v_mfma_i32_16x16x64_i8 v[70:73], v[170:173], v[210:213], v[70:73]
	v_mfma_i32_16x16x64_i8 v[66:69], v[178:181], v[210:213], v[66:69]
	s_setprio 0
	s_barrier
	s_add_i32 s62, s54, s43
	v_lshl_add_u64 v[142:143], s[34:35], 0, v[132:133]
	s_mov_b32 m0, s62
	ds_read_b128 v[182:185], v146 offset:16384
	ds_read_b128 v[186:189], v146 offset:17408
	ds_read_b128 v[190:193], v146 offset:18432
	ds_read_b128 v[194:197], v146 offset:19456
	ds_read_b128 v[198:201], v146 offset:20480
	ds_read_b128 v[202:205], v146 offset:21504
	ds_read_b128 v[206:209], v146 offset:22528
	ds_read_b128 v[210:213], v146 offset:23552
	global_load_lds_dwordx4 v[142:143], off
	s_add_i32 m0, s62, 0x2000
	s_add_u32 s62, s34, 0x40000
	v_lshl_add_u64 v[216:217], s[34:35], 0, v[136:137]
	s_addc_u32 s63, s35, 0
	s_add_i32 s64, s55, s43
	global_load_lds_dwordx4 v[216:217], off
	v_lshl_add_u64 v[218:219], s[62:63], 0, v[132:133]
	s_mov_b32 m0, s64
	v_lshl_add_u64 v[220:221], s[38:39], 0, v[134:135]
	global_load_lds_dwordx4 v[218:219], off
	v_lshl_add_u64 v[218:219], s[62:63], 0, v[136:137]
	s_add_i32 m0, s64, 0x2000
	s_nop 0
	global_load_lds_dwordx4 v[218:219], off
	v_lshl_add_u64 v[218:219], s[38:39], 0, v[130:131]
	s_mov_b32 m0, s29
	s_nop 0
	global_load_lds_dwordx4 v[218:219], off
	s_mov_b32 m0, s44
	s_nop 0
	global_load_lds_dwordx4 v[220:221], off
	s_waitcnt vmcnt(8)
	s_waitcnt lgkmcnt(0)
	s_barrier
	s_setprio 1
	s_waitcnt lgkmcnt(0)
	v_mfma_i32_16x16x64_i8 v[62:65], v[150:153], v[182:185], 0
	v_mfma_i32_16x16x64_i8 v[58:61], v[158:161], v[182:185], 0
	v_mfma_i32_16x16x64_i8 v[50:53], v[150:153], v[190:193], 0
	v_mfma_i32_16x16x64_i8 v[42:45], v[158:161], v[190:193], 0
	v_mfma_i32_16x16x64_i8 v[34:37], v[150:153], v[198:201], 0
	v_mfma_i32_16x16x64_i8 v[26:29], v[158:161], v[198:201], 0
	v_mfma_i32_16x16x64_i8 v[18:21], v[150:153], v[206:209], 0
	v_mfma_i32_16x16x64_i8 v[10:13], v[158:161], v[206:209], 0
	v_mfma_i32_16x16x64_i8 v[62:65], v[154:157], v[186:189], v[62:65]
	v_mfma_i32_16x16x64_i8 v[58:61], v[162:165], v[186:189], v[58:61]
	v_mfma_i32_16x16x64_i8 v[50:53], v[154:157], v[194:197], v[50:53]
	v_mfma_i32_16x16x64_i8 v[42:45], v[162:165], v[194:197], v[42:45]
	v_mfma_i32_16x16x64_i8 v[34:37], v[154:157], v[202:205], v[34:37]
	v_mfma_i32_16x16x64_i8 v[26:29], v[162:165], v[202:205], v[26:29]
	v_mfma_i32_16x16x64_i8 v[18:21], v[154:157], v[210:213], v[18:21]
	v_mfma_i32_16x16x64_i8 v[10:13], v[162:165], v[210:213], v[10:13]
	s_setprio 0
	s_setprio 1
	v_mfma_i32_16x16x64_i8 v[54:57], v[166:169], v[182:185], 0
	v_mfma_i32_16x16x64_i8 v[46:49], v[174:177], v[182:185], 0
	v_mfma_i32_16x16x64_i8 v[38:41], v[166:169], v[190:193], 0
	v_mfma_i32_16x16x64_i8 v[30:33], v[174:177], v[190:193], 0
	v_mfma_i32_16x16x64_i8 v[22:25], v[166:169], v[198:201], 0
	v_mfma_i32_16x16x64_i8 v[14:17], v[174:177], v[198:201], 0
	v_mfma_i32_16x16x64_i8 v[6:9], v[166:169], v[206:209], 0
	v_mfma_i32_16x16x64_i8 v[2:5], v[174:177], v[206:209], 0
	v_mfma_i32_16x16x64_i8 v[54:57], v[170:173], v[186:189], v[54:57]
	v_mfma_i32_16x16x64_i8 v[46:49], v[178:181], v[186:189], v[46:49]
	v_mfma_i32_16x16x64_i8 v[38:41], v[170:173], v[194:197], v[38:41]
	v_mfma_i32_16x16x64_i8 v[30:33], v[178:181], v[194:197], v[30:33]
	v_mfma_i32_16x16x64_i8 v[22:25], v[170:173], v[202:205], v[22:25]
	v_mfma_i32_16x16x64_i8 v[14:17], v[178:181], v[202:205], v[14:17]
	v_mfma_i32_16x16x64_i8 v[6:9], v[170:173], v[210:213], v[6:9]
	v_mfma_i32_16x16x64_i8 v[2:5], v[178:181], v[210:213], v[2:5]
	s_setprio 0
	s_barrier
	s_add_i32 s62, 0, 0x18000
	v_add_u32_e32 v149, s62, v1
	s_add_i32 s63, 0, 0x1c000
	ds_read_b128 v[150:153], v149
	ds_read_b128 v[154:157], v149 offset:1024
	ds_read_b128 v[158:161], v149 offset:2048
	ds_read_b128 v[162:165], v149 offset:3072
	v_add_u32_e32 v149, s63, v1
	ds_read_b128 v[166:169], v149
	ds_read_b128 v[170:173], v149 offset:1024
	ds_read_b128 v[174:177], v149 offset:2048
	ds_read_b128 v[178:181], v149 offset:3072
	s_add_u32 s38, s38, 0x40000
	s_addc_u32 s39, s39, 0
	s_mov_b32 m0, s45
	v_lshl_add_u64 v[222:223], s[38:39], 0, v[130:131]
	ds_read_b128 v[182:185], v146 offset:32768
	ds_read_b128 v[186:189], v146 offset:33792
	ds_read_b128 v[190:193], v146 offset:34816
	ds_read_b128 v[194:197], v146 offset:35840
	ds_read_b128 v[198:201], v146 offset:36864
	ds_read_b128 v[202:205], v146 offset:37888
	ds_read_b128 v[206:209], v146 offset:38912
	ds_read_b128 v[210:213], v146 offset:39936
	global_load_lds_dwordx4 v[222:223], off
	v_lshl_add_u64 v[222:223], s[38:39], 0, v[134:135]
	s_mov_b32 m0, s46
	s_nop 0
	global_load_lds_dwordx4 v[222:223], off
	s_waitcnt vmcnt(8)
	s_waitcnt lgkmcnt(0)
	s_barrier
	s_setprio 1
	s_waitcnt lgkmcnt(0)
	v_mfma_i32_16x16x64_i8 v[126:129], v[150:153], v[182:185], v[126:129]
	v_mfma_i32_16x16x64_i8 v[122:125], v[158:161], v[182:185], v[122:125]
	v_mfma_i32_16x16x64_i8 v[110:113], v[150:153], v[190:193], v[110:113]
	v_mfma_i32_16x16x64_i8 v[106:109], v[158:161], v[190:193], v[106:109]
	v_mfma_i32_16x16x64_i8 v[98:101], v[150:153], v[198:201], v[98:101]
	v_mfma_i32_16x16x64_i8 v[90:93], v[158:161], v[198:201], v[90:93]
	v_mfma_i32_16x16x64_i8 v[82:85], v[150:153], v[206:209], v[82:85]
	v_mfma_i32_16x16x64_i8 v[74:77], v[158:161], v[206:209], v[74:77]
	v_mfma_i32_16x16x64_i8 v[126:129], v[154:157], v[186:189], v[126:129]
	v_mfma_i32_16x16x64_i8 v[122:125], v[162:165], v[186:189], v[122:125]
	v_mfma_i32_16x16x64_i8 v[110:113], v[154:157], v[194:197], v[110:113]
	v_mfma_i32_16x16x64_i8 v[106:109], v[162:165], v[194:197], v[106:109]
	v_mfma_i32_16x16x64_i8 v[98:101], v[154:157], v[202:205], v[98:101]
	v_mfma_i32_16x16x64_i8 v[90:93], v[162:165], v[202:205], v[90:93]
	v_mfma_i32_16x16x64_i8 v[82:85], v[154:157], v[210:213], v[82:85]
	v_mfma_i32_16x16x64_i8 v[74:77], v[162:165], v[210:213], v[74:77]
	s_setprio 0
	s_setprio 1
	v_mfma_i32_16x16x64_i8 v[118:121], v[166:169], v[182:185], v[118:121]
	v_mfma_i32_16x16x64_i8 v[114:117], v[174:177], v[182:185], v[114:117]
	v_mfma_i32_16x16x64_i8 v[102:105], v[166:169], v[190:193], v[102:105]
	v_mfma_i32_16x16x64_i8 v[94:97], v[174:177], v[190:193], v[94:97]
	v_mfma_i32_16x16x64_i8 v[86:89], v[166:169], v[198:201], v[86:89]
	v_mfma_i32_16x16x64_i8 v[78:81], v[174:177], v[198:201], v[78:81]
	v_mfma_i32_16x16x64_i8 v[70:73], v[166:169], v[206:209], v[70:73]
	v_mfma_i32_16x16x64_i8 v[66:69], v[174:177], v[206:209], v[66:69]
	v_mfma_i32_16x16x64_i8 v[118:121], v[170:173], v[186:189], v[118:121]
	v_mfma_i32_16x16x64_i8 v[114:117], v[178:181], v[186:189], v[114:117]
	v_mfma_i32_16x16x64_i8 v[102:105], v[170:173], v[194:197], v[102:105]
	v_mfma_i32_16x16x64_i8 v[94:97], v[178:181], v[194:197], v[94:97]
	v_mfma_i32_16x16x64_i8 v[86:89], v[170:173], v[202:205], v[86:89]
	v_mfma_i32_16x16x64_i8 v[78:81], v[178:181], v[202:205], v[78:81]
	v_mfma_i32_16x16x64_i8 v[70:73], v[170:173], v[210:213], v[70:73]
	v_mfma_i32_16x16x64_i8 v[66:69], v[178:181], v[210:213], v[66:69]
	s_setprio 0
	s_barrier
	s_add_i32 s38, s62, s43
	v_lshl_add_u64 v[142:143], v[142:143], 0, s[12:13]
	s_mov_b32 m0, s38
	ds_read_b128 v[182:185], v146 offset:49152
	ds_read_b128 v[186:189], v146 offset:50176
	ds_read_b128 v[190:193], v146 offset:51200
	ds_read_b128 v[194:197], v146 offset:52224
	ds_read_b128 v[198:201], v146 offset:53248
	ds_read_b128 v[202:205], v146 offset:54272
	ds_read_b128 v[206:209], v146 offset:55296
	ds_read_b128 v[210:213], v146 offset:56320
	global_load_lds_dwordx4 v[142:143], off
	s_add_i32 m0, s38, 0x2000
	s_add_u32 s34, s34, 0x40080
	v_lshl_add_u64 v[142:143], v[216:217], 0, s[12:13]
	s_addc_u32 s35, s35, 0
	s_add_i32 s38, s63, s43
	global_load_lds_dwordx4 v[142:143], off
	v_lshl_add_u64 v[142:143], s[34:35], 0, v[132:133]
	s_mov_b32 m0, s38
	s_nop 0
	global_load_lds_dwordx4 v[142:143], off
	v_lshl_add_u64 v[142:143], s[34:35], 0, v[136:137]
	s_add_i32 m0, s38, 0x2000
	s_nop 0
	global_load_lds_dwordx4 v[142:143], off
	v_lshl_add_u64 v[142:143], v[218:219], 0, s[12:13]
	s_mov_b32 m0, s48
	s_nop 0
	global_load_lds_dwordx4 v[142:143], off
	v_lshl_add_u64 v[142:143], v[220:221], 0, s[12:13]
	s_mov_b32 m0, s49
	s_nop 0
	global_load_lds_dwordx4 v[142:143], off
	s_waitcnt vmcnt(8)
	s_waitcnt lgkmcnt(0)
	s_barrier
	s_setprio 1
	s_waitcnt lgkmcnt(0)
	v_mfma_i32_16x16x64_i8 v[62:65], v[150:153], v[182:185], v[62:65]
	v_mfma_i32_16x16x64_i8 v[58:61], v[158:161], v[182:185], v[58:61]
	v_mfma_i32_16x16x64_i8 v[50:53], v[150:153], v[190:193], v[50:53]
	v_mfma_i32_16x16x64_i8 v[42:45], v[158:161], v[190:193], v[42:45]
	v_mfma_i32_16x16x64_i8 v[34:37], v[150:153], v[198:201], v[34:37]
	v_mfma_i32_16x16x64_i8 v[26:29], v[158:161], v[198:201], v[26:29]
	v_mfma_i32_16x16x64_i8 v[18:21], v[150:153], v[206:209], v[18:21]
	v_mfma_i32_16x16x64_i8 v[10:13], v[158:161], v[206:209], v[10:13]
	v_mfma_i32_16x16x64_i8 v[62:65], v[154:157], v[186:189], v[62:65]
	v_mfma_i32_16x16x64_i8 v[58:61], v[162:165], v[186:189], v[58:61]
	v_mfma_i32_16x16x64_i8 v[50:53], v[154:157], v[194:197], v[50:53]
	v_mfma_i32_16x16x64_i8 v[42:45], v[162:165], v[194:197], v[42:45]
	v_mfma_i32_16x16x64_i8 v[34:37], v[154:157], v[202:205], v[34:37]
	v_mfma_i32_16x16x64_i8 v[26:29], v[162:165], v[202:205], v[26:29]
	v_mfma_i32_16x16x64_i8 v[18:21], v[154:157], v[210:213], v[18:21]
	v_mfma_i32_16x16x64_i8 v[10:13], v[162:165], v[210:213], v[10:13]
	s_setprio 0
	s_setprio 1
	v_mfma_i32_16x16x64_i8 v[54:57], v[166:169], v[182:185], v[54:57]
	v_mfma_i32_16x16x64_i8 v[46:49], v[174:177], v[182:185], v[46:49]
	v_mfma_i32_16x16x64_i8 v[38:41], v[166:169], v[190:193], v[38:41]
	v_mfma_i32_16x16x64_i8 v[30:33], v[174:177], v[190:193], v[30:33]
	v_mfma_i32_16x16x64_i8 v[22:25], v[166:169], v[198:201], v[22:25]
	v_mfma_i32_16x16x64_i8 v[14:17], v[174:177], v[198:201], v[14:17]
	v_mfma_i32_16x16x64_i8 v[6:9], v[166:169], v[206:209], v[6:9]
	v_mfma_i32_16x16x64_i8 v[2:5], v[174:177], v[206:209], v[2:5]
	v_mfma_i32_16x16x64_i8 v[54:57], v[170:173], v[186:189], v[54:57]
	v_mfma_i32_16x16x64_i8 v[46:49], v[178:181], v[186:189], v[46:49]
	v_mfma_i32_16x16x64_i8 v[38:41], v[170:173], v[194:197], v[38:41]
	v_mfma_i32_16x16x64_i8 v[30:33], v[178:181], v[194:197], v[30:33]
	v_mfma_i32_16x16x64_i8 v[22:25], v[170:173], v[202:205], v[22:25]
	v_mfma_i32_16x16x64_i8 v[14:17], v[178:181], v[202:205], v[14:17]
	v_mfma_i32_16x16x64_i8 v[6:9], v[170:173], v[210:213], v[6:9]
	v_mfma_i32_16x16x64_i8 v[2:5], v[178:181], v[210:213], v[2:5]
	s_setprio 0
	s_barrier
	s_add_i32 s61, s61, 2
	s_add_u32 s30, s30, 0x100
	s_addc_u32 s31, s31, 0
	s_add_u32 s59, s59, 0x100
	s_addc_u32 s60, s60, 0
	s_cmp_gt_u32 s61, 13

.LBB0_683:
	s_ashr_i32 s17, s16, 31
	s_xor_b64 s[18:19], s[30:31], -1
	s_lshl_b64 s[20:21], s[16:17], 19
	s_add_u32 s20, s33, s20
	s_addc_u32 s21, s34, s21
	s_and_b64 s[22:23], s[30:31], exec
	s_cselect_b32 s17, s21, s27
	s_cselect_b32 s49, s20, s26
	s_ashr_i32 s15, s14, 31
	s_lshl_b64 s[22:23], s[14:15], 19
	s_add_u32 s22, s35, s22
	s_addc_u32 s23, s38, s23
	s_and_b64 s[30:31], s[30:31], exec
	s_cselect_b32 s15, s23, s29
	s_cselect_b32 s52, s22, s28
	s_add_u32 s26, s26, 0x40080
	s_addc_u32 s27, s27, 0
	s_add_u32 s53, s28, 0x100
	s_addc_u32 s54, s29, 0
	s_mov_b32 s55, -2
	ds_read_b128 v[142:145], v148
	ds_read_b128 v[152:155], v148 offset:1024
	ds_read_b128 v[156:159], v148 offset:2048
	ds_read_b128 v[160:163], v148 offset:3072
	ds_read_b128 v[164:167], v149
	ds_read_b128 v[168:171], v149 offset:1024
	ds_read_b128 v[172:175], v149 offset:2048
	ds_read_b128 v[176:179], v149 offset:3072
	s_add_u32 s28, s26, 0xfffc0080
	s_addc_u32 s29, s27, -1
	s_cmp_eq_u32 s55, 12
	s_cselect_b32 s31, s17, s29
	s_cselect_b32 s30, s49, s28
	s_cselect_b32 s29, s15, s54
	s_cselect_b32 s28, s52, s53
	v_lshl_add_u64 v[146:147], s[26:27], 0, v[138:139]
	s_add_i32 m0, s25, 0xc000
	ds_read_b128 v[180:183], v150
	ds_read_b128 v[184:187], v150 offset:1024
	ds_read_b128 v[188:191], v150 offset:2048
	ds_read_b128 v[192:195], v150 offset:3072
	ds_read_b128 v[196:199], v150 offset:4096
	ds_read_b128 v[200:203], v150 offset:5120
	ds_read_b128 v[204:207], v150 offset:6144
	ds_read_b128 v[208:211], v150 offset:7168
	global_load_lds_dwordx4 v[146:147], off
	v_lshl_add_u64 v[146:147], s[26:27], 0, v[140:141]
	s_add_i32 m0, s25, 0xe000
	s_nop 0
	global_load_lds_dwordx4 v[146:147], off
	s_waitcnt vmcnt(8)
	s_waitcnt lgkmcnt(0)
	s_barrier
	s_setprio 1
	s_waitcnt lgkmcnt(0)
	v_mfma_i32_16x16x64_i8 v[126:129], v[142:145], v[180:183], 0
	v_mfma_i32_16x16x64_i8 v[122:125], v[156:159], v[180:183], 0
	v_mfma_i32_16x16x64_i8 v[110:113], v[142:145], v[188:191], 0
	v_mfma_i32_16x16x64_i8 v[106:109], v[156:159], v[188:191], 0
	v_mfma_i32_16x16x64_i8 v[94:97], v[142:145], v[196:199], 0
	v_mfma_i32_16x16x64_i8 v[90:93], v[156:159], v[196:199], 0
	v_mfma_i32_16x16x64_i8 v[78:81], v[142:145], v[204:207], 0
	v_mfma_i32_16x16x64_i8 v[74:77], v[156:159], v[204:207], 0
	v_mfma_i32_16x16x64_i8 v[126:129], v[152:155], v[184:187], v[126:129]
	v_mfma_i32_16x16x64_i8 v[122:125], v[160:163], v[184:187], v[122:125]
	v_mfma_i32_16x16x64_i8 v[110:113], v[152:155], v[192:195], v[110:113]
	v_mfma_i32_16x16x64_i8 v[106:109], v[160:163], v[192:195], v[106:109]
	v_mfma_i32_16x16x64_i8 v[94:97], v[152:155], v[200:203], v[94:97]
	v_mfma_i32_16x16x64_i8 v[90:93], v[160:163], v[200:203], v[90:93]
	v_mfma_i32_16x16x64_i8 v[78:81], v[152:155], v[208:211], v[78:81]
	v_mfma_i32_16x16x64_i8 v[74:77], v[160:163], v[208:211], v[74:77]
	s_setprio 0
	s_setprio 1
	v_mfma_i32_16x16x64_i8 v[118:121], v[164:167], v[180:183], 0
	v_mfma_i32_16x16x64_i8 v[114:117], v[172:175], v[180:183], 0
	v_mfma_i32_16x16x64_i8 v[102:105], v[164:167], v[188:191], 0
	v_mfma_i32_16x16x64_i8 v[98:101], v[172:175], v[188:191], 0
	v_mfma_i32_16x16x64_i8 v[86:89], v[164:167], v[196:199], 0
	v_mfma_i32_16x16x64_i8 v[82:85], v[172:175], v[196:199], 0
	v_mfma_i32_16x16x64_i8 v[70:73], v[164:167], v[204:207], 0
	v_mfma_i32_16x16x64_i8 v[66:69], v[172:175], v[204:207], 0
	v_mfma_i32_16x16x64_i8 v[118:121], v[168:171], v[184:187], v[118:121]
	v_mfma_i32_16x16x64_i8 v[114:117], v[176:179], v[184:187], v[114:117]
	v_mfma_i32_16x16x64_i8 v[102:105], v[168:171], v[192:195], v[102:105]
	v_mfma_i32_16x16x64_i8 v[98:101], v[176:179], v[192:195], v[98:101]
	v_mfma_i32_16x16x64_i8 v[86:89], v[168:171], v[200:203], v[86:89]
	v_mfma_i32_16x16x64_i8 v[82:85], v[176:179], v[200:203], v[82:85]
	v_mfma_i32_16x16x64_i8 v[70:73], v[168:171], v[208:211], v[70:73]
	v_mfma_i32_16x16x64_i8 v[66:69], v[176:179], v[208:211], v[66:69]
	s_setprio 0
	s_barrier
	s_add_i32 s56, s47, s39
	v_lshl_add_u64 v[146:147], s[28:29], 0, v[132:133]
	s_mov_b32 m0, s56
	ds_read_b128 v[180:183], v150 offset:16384
	ds_read_b128 v[184:187], v150 offset:17408
	ds_read_b128 v[188:191], v150 offset:18432
	ds_read_b128 v[192:195], v150 offset:19456
	ds_read_b128 v[196:199], v150 offset:20480
	ds_read_b128 v[200:203], v150 offset:21504
	ds_read_b128 v[204:207], v150 offset:22528
	ds_read_b128 v[208:211], v150 offset:23552
	global_load_lds_dwordx4 v[146:147], off
	s_add_i32 m0, s56, 0x2000
	s_add_u32 s56, s28, 0x40000
	v_lshl_add_u64 v[212:213], s[28:29], 0, v[136:137]
	s_addc_u32 s57, s29, 0
	s_add_i32 s58, s48, s39
	global_load_lds_dwordx4 v[212:213], off
	v_lshl_add_u64 v[216:217], s[56:57], 0, v[132:133]
	s_mov_b32 m0, s58
	v_lshl_add_u64 v[218:219], s[30:31], 0, v[134:135]
	global_load_lds_dwordx4 v[216:217], off
	v_lshl_add_u64 v[216:217], s[56:57], 0, v[136:137]
	s_add_i32 m0, s58, 0x2000
	s_nop 0
	global_load_lds_dwordx4 v[216:217], off
	v_lshl_add_u64 v[216:217], s[30:31], 0, v[130:131]
	s_mov_b32 m0, s25
	s_nop 0
	global_load_lds_dwordx4 v[216:217], off
	s_mov_b32 m0, s40
	s_nop 0
	global_load_lds_dwordx4 v[218:219], off
	s_waitcnt vmcnt(8)
	s_waitcnt lgkmcnt(0)
	s_barrier
	s_setprio 1
	s_waitcnt lgkmcnt(0)
	v_mfma_i32_16x16x64_i8 v[62:65], v[142:145], v[180:183], 0
	v_mfma_i32_16x16x64_i8 v[58:61], v[156:159], v[180:183], 0
	v_mfma_i32_16x16x64_i8 v[46:49], v[142:145], v[188:191], 0
	v_mfma_i32_16x16x64_i8 v[42:45], v[156:159], v[188:191], 0
	v_mfma_i32_16x16x64_i8 v[30:33], v[142:145], v[196:199], 0
	v_mfma_i32_16x16x64_i8 v[26:29], v[156:159], v[196:199], 0
	v_mfma_i32_16x16x64_i8 v[14:17], v[142:145], v[204:207], 0
	v_mfma_i32_16x16x64_i8 v[10:13], v[156:159], v[204:207], 0
	v_mfma_i32_16x16x64_i8 v[62:65], v[152:155], v[184:187], v[62:65]
	v_mfma_i32_16x16x64_i8 v[58:61], v[160:163], v[184:187], v[58:61]
	v_mfma_i32_16x16x64_i8 v[46:49], v[152:155], v[192:195], v[46:49]
	v_mfma_i32_16x16x64_i8 v[42:45], v[160:163], v[192:195], v[42:45]
	v_mfma_i32_16x16x64_i8 v[30:33], v[152:155], v[200:203], v[30:33]
	v_mfma_i32_16x16x64_i8 v[26:29], v[160:163], v[200:203], v[26:29]
	v_mfma_i32_16x16x64_i8 v[14:17], v[152:155], v[208:211], v[14:17]
	v_mfma_i32_16x16x64_i8 v[10:13], v[160:163], v[208:211], v[10:13]
	s_setprio 0
	s_setprio 1
	v_mfma_i32_16x16x64_i8 v[54:57], v[164:167], v[180:183], 0
	v_mfma_i32_16x16x64_i8 v[50:53], v[172:175], v[180:183], 0
	v_mfma_i32_16x16x64_i8 v[38:41], v[164:167], v[188:191], 0
	v_mfma_i32_16x16x64_i8 v[34:37], v[172:175], v[188:191], 0
	v_mfma_i32_16x16x64_i8 v[22:25], v[164:167], v[196:199], 0
	v_mfma_i32_16x16x64_i8 v[18:21], v[172:175], v[196:199], 0
	v_mfma_i32_16x16x64_i8 v[6:9], v[164:167], v[204:207], 0
	v_mfma_i32_16x16x64_i8 v[2:5], v[172:175], v[204:207], 0
	v_mfma_i32_16x16x64_i8 v[54:57], v[168:171], v[184:187], v[54:57]
	v_mfma_i32_16x16x64_i8 v[50:53], v[176:179], v[184:187], v[50:53]
	v_mfma_i32_16x16x64_i8 v[38:41], v[168:171], v[192:195], v[38:41]
	v_mfma_i32_16x16x64_i8 v[34:37], v[176:179], v[192:195], v[34:37]
	v_mfma_i32_16x16x64_i8 v[22:25], v[168:171], v[200:203], v[22:25]
	v_mfma_i32_16x16x64_i8 v[18:21], v[176:179], v[200:203], v[18:21]
	v_mfma_i32_16x16x64_i8 v[6:9], v[168:171], v[208:211], v[6:9]
	v_mfma_i32_16x16x64_i8 v[2:5], v[176:179], v[208:211], v[2:5]
	s_setprio 0
	s_barrier
	s_add_i32 s56, 0, 0x18000
	s_add_i32 s57, 0, 0x1c000
	v_add_u32_e32 v160, s56, v1
	v_add_u32_e32 v176, s57, v1
	ds_read_b128 v[142:145], v160
	ds_read_b128 v[152:155], v160 offset:1024
	ds_read_b128 v[156:159], v160 offset:2048
	ds_read_b128 v[160:163], v160 offset:3072
	ds_read_b128 v[164:167], v176
	ds_read_b128 v[168:171], v176 offset:1024
	ds_read_b128 v[172:175], v176 offset:2048
	ds_read_b128 v[176:179], v176 offset:3072
	s_add_u32 s30, s30, 0x40000
	s_addc_u32 s31, s31, 0
	s_mov_b32 m0, s41
	v_lshl_add_u64 v[220:221], s[30:31], 0, v[130:131]
	ds_read_b128 v[180:183], v150 offset:32768
	ds_read_b128 v[184:187], v150 offset:33792
	ds_read_b128 v[188:191], v150 offset:34816
	ds_read_b128 v[192:195], v150 offset:35840
	ds_read_b128 v[196:199], v150 offset:36864
	ds_read_b128 v[200:203], v150 offset:37888
	ds_read_b128 v[204:207], v150 offset:38912
	ds_read_b128 v[208:211], v150 offset:39936
	global_load_lds_dwordx4 v[220:221], off
	v_lshl_add_u64 v[220:221], s[30:31], 0, v[134:135]
	s_mov_b32 m0, s42
	s_nop 0
	global_load_lds_dwordx4 v[220:221], off
	s_waitcnt vmcnt(8)
	s_waitcnt lgkmcnt(0)
	s_barrier
	s_setprio 1
	s_waitcnt lgkmcnt(0)
	v_mfma_i32_16x16x64_i8 v[126:129], v[142:145], v[180:183], v[126:129]
	v_mfma_i32_16x16x64_i8 v[122:125], v[156:159], v[180:183], v[122:125]
	v_mfma_i32_16x16x64_i8 v[110:113], v[142:145], v[188:191], v[110:113]
	v_mfma_i32_16x16x64_i8 v[106:109], v[156:159], v[188:191], v[106:109]
	v_mfma_i32_16x16x64_i8 v[94:97], v[142:145], v[196:199], v[94:97]
	v_mfma_i32_16x16x64_i8 v[90:93], v[156:159], v[196:199], v[90:93]
	v_mfma_i32_16x16x64_i8 v[78:81], v[142:145], v[204:207], v[78:81]
	v_mfma_i32_16x16x64_i8 v[74:77], v[156:159], v[204:207], v[74:77]
	v_mfma_i32_16x16x64_i8 v[126:129], v[152:155], v[184:187], v[126:129]
	v_mfma_i32_16x16x64_i8 v[122:125], v[160:163], v[184:187], v[122:125]
	v_mfma_i32_16x16x64_i8 v[110:113], v[152:155], v[192:195], v[110:113]
	v_mfma_i32_16x16x64_i8 v[106:109], v[160:163], v[192:195], v[106:109]
	v_mfma_i32_16x16x64_i8 v[94:97], v[152:155], v[200:203], v[94:97]
	v_mfma_i32_16x16x64_i8 v[90:93], v[160:163], v[200:203], v[90:93]
	v_mfma_i32_16x16x64_i8 v[78:81], v[152:155], v[208:211], v[78:81]
	v_mfma_i32_16x16x64_i8 v[74:77], v[160:163], v[208:211], v[74:77]
	s_setprio 0
	s_setprio 1
	v_mfma_i32_16x16x64_i8 v[118:121], v[164:167], v[180:183], v[118:121]
	v_mfma_i32_16x16x64_i8 v[114:117], v[172:175], v[180:183], v[114:117]
	v_mfma_i32_16x16x64_i8 v[102:105], v[164:167], v[188:191], v[102:105]
	v_mfma_i32_16x16x64_i8 v[98:101], v[172:175], v[188:191], v[98:101]
	v_mfma_i32_16x16x64_i8 v[86:89], v[164:167], v[196:199], v[86:89]
	v_mfma_i32_16x16x64_i8 v[82:85], v[172:175], v[196:199], v[82:85]
	v_mfma_i32_16x16x64_i8 v[70:73], v[164:167], v[204:207], v[70:73]
	v_mfma_i32_16x16x64_i8 v[66:69], v[172:175], v[204:207], v[66:69]
	v_mfma_i32_16x16x64_i8 v[118:121], v[168:171], v[184:187], v[118:121]
	v_mfma_i32_16x16x64_i8 v[114:117], v[176:179], v[184:187], v[114:117]
	v_mfma_i32_16x16x64_i8 v[102:105], v[168:171], v[192:195], v[102:105]
	v_mfma_i32_16x16x64_i8 v[98:101], v[176:179], v[192:195], v[98:101]
	v_mfma_i32_16x16x64_i8 v[86:89], v[168:171], v[200:203], v[86:89]
	v_mfma_i32_16x16x64_i8 v[82:85], v[176:179], v[200:203], v[82:85]
	v_mfma_i32_16x16x64_i8 v[70:73], v[168:171], v[208:211], v[70:73]
	v_mfma_i32_16x16x64_i8 v[66:69], v[176:179], v[208:211], v[66:69]
	s_setprio 0
	s_barrier
	s_add_i32 s30, s56, s39
	v_lshl_add_u64 v[146:147], v[146:147], 0, s[10:11]
	s_mov_b32 m0, s30
	ds_read_b128 v[180:183], v150 offset:49152
	ds_read_b128 v[184:187], v150 offset:50176
	ds_read_b128 v[188:191], v150 offset:51200
	ds_read_b128 v[192:195], v150 offset:52224
	ds_read_b128 v[196:199], v150 offset:53248
	ds_read_b128 v[200:203], v150 offset:54272
	ds_read_b128 v[204:207], v150 offset:55296
	ds_read_b128 v[208:211], v150 offset:56320
	global_load_lds_dwordx4 v[146:147], off
	s_add_i32 m0, s30, 0x2000
	s_add_u32 s28, s28, 0x40080
	v_lshl_add_u64 v[146:147], v[212:213], 0, s[10:11]
	s_addc_u32 s29, s29, 0
	s_add_i32 s30, s57, s39
	global_load_lds_dwordx4 v[146:147], off
	v_lshl_add_u64 v[146:147], s[28:29], 0, v[132:133]
	s_mov_b32 m0, s30
	s_nop 0
	global_load_lds_dwordx4 v[146:147], off
	v_lshl_add_u64 v[146:147], s[28:29], 0, v[136:137]
	s_add_i32 m0, s30, 0x2000
	s_nop 0
	global_load_lds_dwordx4 v[146:147], off
	v_lshl_add_u64 v[146:147], v[216:217], 0, s[10:11]
	s_mov_b32 m0, s45
	s_nop 0
	global_load_lds_dwordx4 v[146:147], off
	v_lshl_add_u64 v[146:147], v[218:219], 0, s[10:11]
	s_mov_b32 m0, s46
	s_nop 0
	global_load_lds_dwordx4 v[146:147], off
	s_waitcnt vmcnt(8)
	s_waitcnt lgkmcnt(0)
	s_barrier
	s_setprio 1
	s_waitcnt lgkmcnt(0)
	v_mfma_i32_16x16x64_i8 v[62:65], v[142:145], v[180:183], v[62:65]
	v_mfma_i32_16x16x64_i8 v[58:61], v[156:159], v[180:183], v[58:61]
	v_mfma_i32_16x16x64_i8 v[46:49], v[142:145], v[188:191], v[46:49]
	v_mfma_i32_16x16x64_i8 v[42:45], v[156:159], v[188:191], v[42:45]
	v_mfma_i32_16x16x64_i8 v[30:33], v[142:145], v[196:199], v[30:33]
	v_mfma_i32_16x16x64_i8 v[26:29], v[156:159], v[196:199], v[26:29]
	v_mfma_i32_16x16x64_i8 v[14:17], v[142:145], v[204:207], v[14:17]
	v_mfma_i32_16x16x64_i8 v[10:13], v[156:159], v[204:207], v[10:13]
	v_mfma_i32_16x16x64_i8 v[62:65], v[152:155], v[184:187], v[62:65]
	v_mfma_i32_16x16x64_i8 v[58:61], v[160:163], v[184:187], v[58:61]
	v_mfma_i32_16x16x64_i8 v[46:49], v[152:155], v[192:195], v[46:49]
	v_mfma_i32_16x16x64_i8 v[42:45], v[160:163], v[192:195], v[42:45]
	v_mfma_i32_16x16x64_i8 v[30:33], v[152:155], v[200:203], v[30:33]
	v_mfma_i32_16x16x64_i8 v[26:29], v[160:163], v[200:203], v[26:29]
	v_mfma_i32_16x16x64_i8 v[14:17], v[152:155], v[208:211], v[14:17]
	v_mfma_i32_16x16x64_i8 v[10:13], v[160:163], v[208:211], v[10:13]
	s_setprio 0
	s_setprio 1
	v_mfma_i32_16x16x64_i8 v[54:57], v[164:167], v[180:183], v[54:57]
	v_mfma_i32_16x16x64_i8 v[50:53], v[172:175], v[180:183], v[50:53]
	v_mfma_i32_16x16x64_i8 v[38:41], v[164:167], v[188:191], v[38:41]
	v_mfma_i32_16x16x64_i8 v[34:37], v[172:175], v[188:191], v[34:37]
	v_mfma_i32_16x16x64_i8 v[22:25], v[164:167], v[196:199], v[22:25]
	v_mfma_i32_16x16x64_i8 v[18:21], v[172:175], v[196:199], v[18:21]
	v_mfma_i32_16x16x64_i8 v[6:9], v[164:167], v[204:207], v[6:9]
	v_mfma_i32_16x16x64_i8 v[2:5], v[172:175], v[204:207], v[2:5]
	v_mfma_i32_16x16x64_i8 v[54:57], v[168:171], v[184:187], v[54:57]
	v_mfma_i32_16x16x64_i8 v[50:53], v[176:179], v[184:187], v[50:53]
	v_mfma_i32_16x16x64_i8 v[38:41], v[168:171], v[192:195], v[38:41]
	v_mfma_i32_16x16x64_i8 v[34:37], v[176:179], v[192:195], v[34:37]
	v_mfma_i32_16x16x64_i8 v[22:25], v[168:171], v[200:203], v[22:25]
	v_mfma_i32_16x16x64_i8 v[18:21], v[176:179], v[200:203], v[18:21]
	v_mfma_i32_16x16x64_i8 v[6:9], v[168:171], v[208:211], v[6:9]
	v_mfma_i32_16x16x64_i8 v[2:5], v[176:179], v[208:211], v[2:5]
	s_setprio 0
	s_barrier
	s_add_i32 s55, s55, 2
	s_add_u32 s26, s26, 0x100
	s_addc_u32 s27, s27, 0
	s_add_u32 s53, s53, 0x100
	s_addc_u32 s54, s54, 0
	s_cmp_gt_u32 s55, 13

.LBB0_960:
	s_and_b64 vcc, exec, s[4:5]
	s_cbranch_vccz .LBB0_963
	s_add_u32 s0, s30, 0x40080
	s_addc_u32 s1, s31, 0
	s_mov_b32 s34, -2
	s_add_u32 s4, s0, 0xfffc0080
	s_addc_u32 s5, s1, -1
	s_add_i32 s8, 0, 0x10000
	s_cmp_eq_u32 s34, 12
	s_cselect_b32 s31, s21, s5
	s_cselect_b32 s30, s33, s4
	v_add_u32_e32 v3, s8, v216
	s_cselect_b32 s5, s23, s93
	s_cselect_b32 s4, s91, s92
	s_add_i32 s18, 0, 0x14000
	s_waitcnt lgkmcnt(0)
	ds_read_b128 v[126:129], v3
	ds_read_b128 v[130:133], v3 offset:1024
	ds_read_b128 v[142:145], v3 offset:2048
	ds_read_b128 v[146:149], v3 offset:3072
	v_add_u32_e32 v3, s18, v216
	ds_read_b128 v[150:153], v3
	ds_read_b128 v[154:157], v3 offset:1024
	ds_read_b128 v[158:161], v3 offset:2048
	ds_read_b128 v[162:165], v3 offset:3072
	v_lshl_add_u64 v[4:5], s[0:1], 0, v[206:207]
	s_add_i32 m0, s3, 0xc000
	ds_read_b128 v[166:169], v220
	ds_read_b128 v[170:173], v220 offset:1024
	ds_read_b128 v[174:177], v220 offset:2048
	ds_read_b128 v[178:181], v220 offset:3072
	ds_read_b128 v[182:185], v220 offset:4096
	ds_read_b128 v[186:189], v220 offset:5120
	ds_read_b128 v[190:193], v220 offset:6144
	ds_read_b128 v[194:197], v220 offset:7168
	global_load_lds_dwordx4 v[4:5], off
	v_lshl_add_u64 v[4:5], s[0:1], 0, v[204:205]
	s_add_i32 m0, s3, 0xe000
	s_nop 0
	global_load_lds_dwordx4 v[4:5], off
	s_waitcnt vmcnt(8)
	s_waitcnt lgkmcnt(0)
	s_barrier
	s_setprio 1
	s_waitcnt lgkmcnt(0)
	v_mfma_i32_16x16x64_i8 v[138:141], v[126:129], v[166:169], 0
	v_mfma_i32_16x16x64_i8 v[122:125], v[142:145], v[166:169], 0
	v_mfma_i32_16x16x64_i8 v[114:117], v[126:129], v[174:177], 0
	v_mfma_i32_16x16x64_i8 v[106:109], v[142:145], v[174:177], 0
	v_mfma_i32_16x16x64_i8 v[98:101], v[126:129], v[182:185], 0
	v_mfma_i32_16x16x64_i8 v[90:93], v[142:145], v[182:185], 0
	v_mfma_i32_16x16x64_i8 v[82:85], v[126:129], v[190:193], 0
	v_mfma_i32_16x16x64_i8 v[74:77], v[142:145], v[190:193], 0
	v_mfma_i32_16x16x64_i8 v[138:141], v[130:133], v[170:173], v[138:141]
	v_mfma_i32_16x16x64_i8 v[122:125], v[146:149], v[170:173], v[122:125]
	v_mfma_i32_16x16x64_i8 v[114:117], v[130:133], v[178:181], v[114:117]
	v_mfma_i32_16x16x64_i8 v[106:109], v[146:149], v[178:181], v[106:109]
	v_mfma_i32_16x16x64_i8 v[98:101], v[130:133], v[186:189], v[98:101]
	v_mfma_i32_16x16x64_i8 v[90:93], v[146:149], v[186:189], v[90:93]
	v_mfma_i32_16x16x64_i8 v[82:85], v[130:133], v[194:197], v[82:85]
	v_mfma_i32_16x16x64_i8 v[74:77], v[146:149], v[194:197], v[74:77]
	s_setprio 0
	s_setprio 1
	v_mfma_i32_16x16x64_i8 v[134:137], v[150:153], v[166:169], 0
	v_mfma_i32_16x16x64_i8 v[118:121], v[158:161], v[166:169], 0
	v_mfma_i32_16x16x64_i8 v[110:113], v[150:153], v[174:177], 0
	v_mfma_i32_16x16x64_i8 v[102:105], v[158:161], v[174:177], 0
	v_mfma_i32_16x16x64_i8 v[94:97], v[150:153], v[182:185], 0
	v_mfma_i32_16x16x64_i8 v[86:89], v[158:161], v[182:185], 0
	v_mfma_i32_16x16x64_i8 v[78:81], v[150:153], v[190:193], 0
	v_mfma_i32_16x16x64_i8 v[70:73], v[158:161], v[190:193], 0
	v_mfma_i32_16x16x64_i8 v[134:137], v[154:157], v[170:173], v[134:137]
	v_mfma_i32_16x16x64_i8 v[118:121], v[162:165], v[170:173], v[118:121]
	v_mfma_i32_16x16x64_i8 v[110:113], v[154:157], v[178:181], v[110:113]
	v_mfma_i32_16x16x64_i8 v[102:105], v[162:165], v[178:181], v[102:105]
	v_mfma_i32_16x16x64_i8 v[94:97], v[154:157], v[186:189], v[94:97]
	v_mfma_i32_16x16x64_i8 v[86:89], v[162:165], v[186:189], v[86:89]
	v_mfma_i32_16x16x64_i8 v[78:81], v[154:157], v[194:197], v[78:81]
	v_mfma_i32_16x16x64_i8 v[70:73], v[162:165], v[194:197], v[70:73]
	s_setprio 0
	s_barrier
	s_add_i32 s8, s8, s54
	v_lshl_add_u64 v[208:209], s[4:5], 0, v[198:199]
	s_mov_b32 m0, s8
	ds_read_b128 v[166:169], v220 offset:16384
	ds_read_b128 v[170:173], v220 offset:17408
	ds_read_b128 v[174:177], v220 offset:18432
	ds_read_b128 v[178:181], v220 offset:19456
	ds_read_b128 v[182:185], v220 offset:20480
	ds_read_b128 v[186:189], v220 offset:21504
	ds_read_b128 v[190:193], v220 offset:22528
	ds_read_b128 v[194:197], v220 offset:23552
	global_load_lds_dwordx4 v[208:209], off
	s_add_i32 m0, s8, 0x2000
	s_add_u32 s8, s4, 0x40000
	v_lshl_add_u64 v[210:211], s[4:5], 0, v[200:201]
	s_addc_u32 s9, s5, 0
	s_add_i32 s18, s18, s54
	global_load_lds_dwordx4 v[210:211], off
	v_lshl_add_u64 v[4:5], s[8:9], 0, v[198:199]
	s_mov_b32 m0, s18
	v_lshl_add_u64 v[212:213], s[30:31], 0, v[202:203]
	global_load_lds_dwordx4 v[4:5], off
	v_lshl_add_u64 v[4:5], s[8:9], 0, v[200:201]
	s_add_i32 m0, s18, 0x2000
	v_lshl_add_u64 v[226:227], s[30:31], 0, v[204:205]
	global_load_lds_dwordx4 v[4:5], off
	s_mov_b32 m0, s3
	s_nop 0
	global_load_lds_dwordx4 v[212:213], off
	s_add_i32 m0, s3, 0x2000
	s_nop 0
	global_load_lds_dwordx4 v[226:227], off
	s_waitcnt vmcnt(8)
	s_waitcnt lgkmcnt(0)
	s_barrier
	s_setprio 1
	s_waitcnt lgkmcnt(0)
	v_mfma_i32_16x16x64_i8 v[66:69], v[126:129], v[166:169], 0
	v_mfma_i32_16x16x64_i8 v[58:61], v[142:145], v[166:169], 0
	v_mfma_i32_16x16x64_i8 v[50:53], v[126:129], v[174:177], 0
	v_mfma_i32_16x16x64_i8 v[42:45], v[142:145], v[174:177], 0
	v_mfma_i32_16x16x64_i8 v[34:37], v[126:129], v[182:185], 0
	v_mfma_i32_16x16x64_i8 v[26:29], v[142:145], v[182:185], 0
	v_mfma_i32_16x16x64_i8 v[18:21], v[126:129], v[190:193], 0
	v_mfma_i32_16x16x64_i8 v[10:13], v[142:145], v[190:193], 0
	v_mfma_i32_16x16x64_i8 v[66:69], v[130:133], v[170:173], v[66:69]
	v_mfma_i32_16x16x64_i8 v[58:61], v[146:149], v[170:173], v[58:61]
	v_mfma_i32_16x16x64_i8 v[50:53], v[130:133], v[178:181], v[50:53]
	v_mfma_i32_16x16x64_i8 v[42:45], v[146:149], v[178:181], v[42:45]
	v_mfma_i32_16x16x64_i8 v[34:37], v[130:133], v[186:189], v[34:37]
	v_mfma_i32_16x16x64_i8 v[26:29], v[146:149], v[186:189], v[26:29]
	v_mfma_i32_16x16x64_i8 v[18:21], v[130:133], v[194:197], v[18:21]
	v_mfma_i32_16x16x64_i8 v[10:13], v[146:149], v[194:197], v[10:13]
	s_setprio 0
	s_setprio 1
	v_mfma_i32_16x16x64_i8 v[62:65], v[150:153], v[166:169], 0
	v_mfma_i32_16x16x64_i8 v[54:57], v[158:161], v[166:169], 0
	v_mfma_i32_16x16x64_i8 v[46:49], v[150:153], v[174:177], 0
	v_mfma_i32_16x16x64_i8 v[38:41], v[158:161], v[174:177], 0
	v_mfma_i32_16x16x64_i8 v[30:33], v[150:153], v[182:185], 0
	v_mfma_i32_16x16x64_i8 v[22:25], v[158:161], v[182:185], 0
	v_mfma_i32_16x16x64_i8 v[14:17], v[150:153], v[190:193], 0
	v_mfma_i32_16x16x64_i8 v[4:7], v[158:161], v[190:193], 0
	v_mfma_i32_16x16x64_i8 v[62:65], v[154:157], v[170:173], v[62:65]
	v_mfma_i32_16x16x64_i8 v[54:57], v[162:165], v[170:173], v[54:57]
	v_mfma_i32_16x16x64_i8 v[46:49], v[154:157], v[178:181], v[46:49]
	v_mfma_i32_16x16x64_i8 v[38:41], v[162:165], v[178:181], v[38:41]
	v_mfma_i32_16x16x64_i8 v[30:33], v[154:157], v[186:189], v[30:33]
	v_mfma_i32_16x16x64_i8 v[22:25], v[162:165], v[186:189], v[22:25]
	v_mfma_i32_16x16x64_i8 v[14:17], v[154:157], v[194:197], v[14:17]
	v_mfma_i32_16x16x64_i8 v[4:7], v[162:165], v[194:197], v[4:7]
	s_setprio 0
	s_barrier
	s_add_i32 s18, 0, 0x18000
	v_add_u32_e32 v3, s18, v216
	s_add_i32 s19, 0, 0x1c000
	ds_read_b128 v[126:129], v3
	ds_read_b128 v[130:133], v3 offset:1024
	ds_read_b128 v[142:145], v3 offset:2048
	ds_read_b128 v[146:149], v3 offset:3072
	v_add_u32_e32 v3, s19, v216
	ds_read_b128 v[150:153], v3
	ds_read_b128 v[154:157], v3 offset:1024
	ds_read_b128 v[158:161], v3 offset:2048
	ds_read_b128 v[162:165], v3 offset:3072
	s_add_u32 s8, s30, 0x40000
	s_addc_u32 s9, s31, 0
	v_lshl_add_u64 v[8:9], s[8:9], 0, v[202:203]
	s_add_i32 m0, s3, 0x4000
	ds_read_b128 v[166:169], v220 offset:32768
	ds_read_b128 v[170:173], v220 offset:33792
	ds_read_b128 v[174:177], v220 offset:34816
	ds_read_b128 v[178:181], v220 offset:35840
	ds_read_b128 v[182:185], v220 offset:36864
	ds_read_b128 v[186:189], v220 offset:37888
	ds_read_b128 v[190:193], v220 offset:38912
	ds_read_b128 v[194:197], v220 offset:39936
	global_load_lds_dwordx4 v[8:9], off
	v_lshl_add_u64 v[8:9], s[8:9], 0, v[204:205]
	s_add_i32 m0, s3, 0x6000
	s_nop 0
	global_load_lds_dwordx4 v[8:9], off
	s_waitcnt vmcnt(8)
	s_waitcnt lgkmcnt(0)
	s_barrier
	s_setprio 1
	s_waitcnt lgkmcnt(0)
	v_mfma_i32_16x16x64_i8 v[138:141], v[126:129], v[166:169], v[138:141]
	v_mfma_i32_16x16x64_i8 v[122:125], v[142:145], v[166:169], v[122:125]
	v_mfma_i32_16x16x64_i8 v[114:117], v[126:129], v[174:177], v[114:117]
	v_mfma_i32_16x16x64_i8 v[106:109], v[142:145], v[174:177], v[106:109]
	v_mfma_i32_16x16x64_i8 v[98:101], v[126:129], v[182:185], v[98:101]
	v_mfma_i32_16x16x64_i8 v[90:93], v[142:145], v[182:185], v[90:93]
	v_mfma_i32_16x16x64_i8 v[82:85], v[126:129], v[190:193], v[82:85]
	v_mfma_i32_16x16x64_i8 v[74:77], v[142:145], v[190:193], v[74:77]
	v_mfma_i32_16x16x64_i8 v[138:141], v[130:133], v[170:173], v[138:141]
	v_mfma_i32_16x16x64_i8 v[122:125], v[146:149], v[170:173], v[122:125]
	v_mfma_i32_16x16x64_i8 v[114:117], v[130:133], v[178:181], v[114:117]
	v_mfma_i32_16x16x64_i8 v[106:109], v[146:149], v[178:181], v[106:109]
	v_mfma_i32_16x16x64_i8 v[98:101], v[130:133], v[186:189], v[98:101]
	v_mfma_i32_16x16x64_i8 v[90:93], v[146:149], v[186:189], v[90:93]
	v_mfma_i32_16x16x64_i8 v[82:85], v[130:133], v[194:197], v[82:85]
	v_mfma_i32_16x16x64_i8 v[74:77], v[146:149], v[194:197], v[74:77]
	s_setprio 0
	s_setprio 1
	v_mfma_i32_16x16x64_i8 v[134:137], v[150:153], v[166:169], v[134:137]
	v_mfma_i32_16x16x64_i8 v[118:121], v[158:161], v[166:169], v[118:121]
	v_mfma_i32_16x16x64_i8 v[110:113], v[150:153], v[174:177], v[110:113]
	v_mfma_i32_16x16x64_i8 v[102:105], v[158:161], v[174:177], v[102:105]
	v_mfma_i32_16x16x64_i8 v[94:97], v[150:153], v[182:185], v[94:97]
	v_mfma_i32_16x16x64_i8 v[86:89], v[158:161], v[182:185], v[86:89]
	v_mfma_i32_16x16x64_i8 v[78:81], v[150:153], v[190:193], v[78:81]
	v_mfma_i32_16x16x64_i8 v[70:73], v[158:161], v[190:193], v[70:73]
	v_mfma_i32_16x16x64_i8 v[134:137], v[154:157], v[170:173], v[134:137]
	v_mfma_i32_16x16x64_i8 v[118:121], v[162:165], v[170:173], v[118:121]
	v_mfma_i32_16x16x64_i8 v[110:113], v[154:157], v[178:181], v[110:113]
	v_mfma_i32_16x16x64_i8 v[102:105], v[162:165], v[178:181], v[102:105]
	v_mfma_i32_16x16x64_i8 v[94:97], v[154:157], v[186:189], v[94:97]
	v_mfma_i32_16x16x64_i8 v[86:89], v[162:165], v[186:189], v[86:89]
	v_mfma_i32_16x16x64_i8 v[78:81], v[154:157], v[194:197], v[78:81]
	v_mfma_i32_16x16x64_i8 v[70:73], v[162:165], v[194:197], v[70:73]
	s_setprio 0
	s_barrier
	s_add_i32 s8, s18, s54
	v_lshl_add_u64 v[8:9], v[208:209], 0, s[16:17]
	s_mov_b32 m0, s8
	ds_read_b128 v[166:169], v220 offset:49152
	ds_read_b128 v[170:173], v220 offset:50176
	ds_read_b128 v[174:177], v220 offset:51200
	ds_read_b128 v[178:181], v220 offset:52224
	ds_read_b128 v[182:185], v220 offset:53248
	ds_read_b128 v[186:189], v220 offset:54272
	ds_read_b128 v[190:193], v220 offset:55296
	ds_read_b128 v[194:197], v220 offset:56320
	global_load_lds_dwordx4 v[8:9], off
	s_add_i32 m0, s8, 0x2000
	s_add_u32 s4, s4, 0x40080
	v_lshl_add_u64 v[8:9], v[210:211], 0, s[16:17]
	s_addc_u32 s5, s5, 0
	s_add_i32 s8, s19, s54
	global_load_lds_dwordx4 v[8:9], off
	v_lshl_add_u64 v[8:9], s[4:5], 0, v[198:199]
	s_mov_b32 m0, s8
	s_nop 0
	global_load_lds_dwordx4 v[8:9], off
	v_lshl_add_u64 v[8:9], s[4:5], 0, v[200:201]
	s_add_i32 m0, s8, 0x2000
	s_nop 0
	global_load_lds_dwordx4 v[8:9], off
	v_lshl_add_u64 v[8:9], v[212:213], 0, s[16:17]
	s_add_i32 m0, s3, 0x8000
	s_nop 0
	global_load_lds_dwordx4 v[8:9], off
	v_lshl_add_u64 v[8:9], v[226:227], 0, s[16:17]
	s_add_i32 m0, s3, 0xa000
	s_nop 0
	global_load_lds_dwordx4 v[8:9], off
	s_waitcnt vmcnt(8)
	s_waitcnt lgkmcnt(0)
	s_barrier
	s_setprio 1
	s_waitcnt lgkmcnt(0)
	v_mfma_i32_16x16x64_i8 v[66:69], v[126:129], v[166:169], v[66:69]
	v_mfma_i32_16x16x64_i8 v[58:61], v[142:145], v[166:169], v[58:61]
	v_mfma_i32_16x16x64_i8 v[50:53], v[126:129], v[174:177], v[50:53]
	v_mfma_i32_16x16x64_i8 v[42:45], v[142:145], v[174:177], v[42:45]
	v_mfma_i32_16x16x64_i8 v[34:37], v[126:129], v[182:185], v[34:37]
	v_mfma_i32_16x16x64_i8 v[26:29], v[142:145], v[182:185], v[26:29]
	v_mfma_i32_16x16x64_i8 v[18:21], v[126:129], v[190:193], v[18:21]
	v_mfma_i32_16x16x64_i8 v[8:11], v[142:145], v[190:193], v[10:13]
	v_mfma_i32_16x16x64_i8 v[66:69], v[130:133], v[170:173], v[66:69]
	v_mfma_i32_16x16x64_i8 v[58:61], v[146:149], v[170:173], v[58:61]
	v_mfma_i32_16x16x64_i8 v[50:53], v[130:133], v[178:181], v[50:53]
	v_mfma_i32_16x16x64_i8 v[42:45], v[146:149], v[178:181], v[42:45]
	v_mfma_i32_16x16x64_i8 v[34:37], v[130:133], v[186:189], v[34:37]
	v_mfma_i32_16x16x64_i8 v[26:29], v[146:149], v[186:189], v[26:29]
	v_mfma_i32_16x16x64_i8 v[18:21], v[130:133], v[194:197], v[18:21]
	v_mfma_i32_16x16x64_i8 v[10:13], v[146:149], v[194:197], v[8:11]
	s_setprio 0
	s_setprio 1
	v_mfma_i32_16x16x64_i8 v[62:65], v[150:153], v[166:169], v[62:65]
	v_mfma_i32_16x16x64_i8 v[54:57], v[158:161], v[166:169], v[54:57]
	v_mfma_i32_16x16x64_i8 v[46:49], v[150:153], v[174:177], v[46:49]
	v_mfma_i32_16x16x64_i8 v[38:41], v[158:161], v[174:177], v[38:41]
	v_mfma_i32_16x16x64_i8 v[30:33], v[150:153], v[182:185], v[30:33]
	v_mfma_i32_16x16x64_i8 v[22:25], v[158:161], v[182:185], v[22:25]
	v_mfma_i32_16x16x64_i8 v[14:17], v[150:153], v[190:193], v[14:17]
	v_mfma_i32_16x16x64_i8 v[4:7], v[158:161], v[190:193], v[4:7]
	v_mfma_i32_16x16x64_i8 v[62:65], v[154:157], v[170:173], v[62:65]
	v_mfma_i32_16x16x64_i8 v[54:57], v[162:165], v[170:173], v[54:57]
	v_mfma_i32_16x16x64_i8 v[46:49], v[154:157], v[178:181], v[46:49]
	v_mfma_i32_16x16x64_i8 v[38:41], v[162:165], v[178:181], v[38:41]
	v_mfma_i32_16x16x64_i8 v[30:33], v[154:157], v[186:189], v[30:33]
	v_mfma_i32_16x16x64_i8 v[22:25], v[162:165], v[186:189], v[22:25]
	v_mfma_i32_16x16x64_i8 v[14:17], v[154:157], v[194:197], v[14:17]
	v_mfma_i32_16x16x64_i8 v[6:9], v[162:165], v[194:197], v[4:7]
	s_setprio 0
	s_barrier
	s_add_i32 s34, s34, 2
	s_add_u32 s0, s0, 0x100
	s_addc_u32 s1, s1, 0
	s_add_u32 s92, s92, 0x100
	s_addc_u32 s93, s93, 0
	s_cmp_gt_u32 s34, 13

.LBB0_1123:
	s_and_b64 vcc, exec, s[4:5]
	s_cbranch_vccz .LBB0_1126
	s_add_u32 s0, s8, 0x40080
	s_addc_u32 s1, s9, 0
	s_mov_b32 s10, -2
	s_add_u32 s4, s0, 0xfffc0080
	s_addc_u32 s5, s1, -1
	s_add_i32 s11, 0, 0x10000
	s_cmp_eq_u32 s10, 12
	s_cselect_b32 s9, s3, s5
	s_cselect_b32 s8, s7, s4
	v_add_u32_e32 v3, s11, v212
	s_cselect_b32 s5, s33, s81
	s_cselect_b32 s4, s35, s37
	s_add_i32 s14, 0, 0x14000
	s_waitcnt lgkmcnt(0)
	ds_read_b128 v[134:137], v3
	ds_read_b128 v[138:141], v3 offset:1024
	ds_read_b128 v[142:145], v3 offset:2048
	ds_read_b128 v[146:149], v3 offset:3072
	v_add_u32_e32 v3, s14, v212
	ds_read_b128 v[150:153], v3
	ds_read_b128 v[154:157], v3 offset:1024
	ds_read_b128 v[158:161], v3 offset:2048
	ds_read_b128 v[162:165], v3 offset:3072
	v_lshl_add_u64 v[4:5], s[0:1], 0, v[0:1]
	s_add_i32 m0, s60, 0xc000
	ds_read_b128 v[166:169], v217
	ds_read_b128 v[170:173], v217 offset:1024
	ds_read_b128 v[174:177], v217 offset:2048
	ds_read_b128 v[178:181], v217 offset:3072
	ds_read_b128 v[182:185], v217 offset:4096
	ds_read_b128 v[186:189], v217 offset:5120
	ds_read_b128 v[190:193], v217 offset:6144
	ds_read_b128 v[194:197], v217 offset:7168
	global_load_lds_dwordx4 v[4:5], off
	v_lshl_add_u64 v[4:5], s[0:1], 0, v[204:205]
	s_add_i32 m0, s60, 0xe000
	s_nop 0
	global_load_lds_dwordx4 v[4:5], off
	s_waitcnt vmcnt(8)
	s_waitcnt lgkmcnt(0)
	s_barrier
	s_setprio 1
	s_waitcnt lgkmcnt(0)
	v_mfma_i32_16x16x64_i8 v[130:133], v[134:137], v[166:169], 0
	v_mfma_i32_16x16x64_i8 v[126:129], v[142:145], v[166:169], 0
	v_mfma_i32_16x16x64_i8 v[114:117], v[134:137], v[174:177], 0
	v_mfma_i32_16x16x64_i8 v[110:113], v[142:145], v[174:177], 0
	v_mfma_i32_16x16x64_i8 v[98:101], v[134:137], v[182:185], 0
	v_mfma_i32_16x16x64_i8 v[94:97], v[142:145], v[182:185], 0
	v_mfma_i32_16x16x64_i8 v[82:85], v[134:137], v[190:193], 0
	v_mfma_i32_16x16x64_i8 v[78:81], v[142:145], v[190:193], 0
	v_mfma_i32_16x16x64_i8 v[130:133], v[138:141], v[170:173], v[130:133]
	v_mfma_i32_16x16x64_i8 v[126:129], v[146:149], v[170:173], v[126:129]
	v_mfma_i32_16x16x64_i8 v[114:117], v[138:141], v[178:181], v[114:117]
	v_mfma_i32_16x16x64_i8 v[110:113], v[146:149], v[178:181], v[110:113]
	v_mfma_i32_16x16x64_i8 v[98:101], v[138:141], v[186:189], v[98:101]
	v_mfma_i32_16x16x64_i8 v[94:97], v[146:149], v[186:189], v[94:97]
	v_mfma_i32_16x16x64_i8 v[82:85], v[138:141], v[194:197], v[82:85]
	v_mfma_i32_16x16x64_i8 v[78:81], v[146:149], v[194:197], v[78:81]
	s_setprio 0
	s_setprio 1
	v_mfma_i32_16x16x64_i8 v[122:125], v[150:153], v[166:169], 0
	v_mfma_i32_16x16x64_i8 v[118:121], v[158:161], v[166:169], 0
	v_mfma_i32_16x16x64_i8 v[106:109], v[150:153], v[174:177], 0
	v_mfma_i32_16x16x64_i8 v[102:105], v[158:161], v[174:177], 0
	v_mfma_i32_16x16x64_i8 v[90:93], v[150:153], v[182:185], 0
	v_mfma_i32_16x16x64_i8 v[86:89], v[158:161], v[182:185], 0
	v_mfma_i32_16x16x64_i8 v[74:77], v[150:153], v[190:193], 0
	v_mfma_i32_16x16x64_i8 v[70:73], v[158:161], v[190:193], 0
	v_mfma_i32_16x16x64_i8 v[122:125], v[154:157], v[170:173], v[122:125]
	v_mfma_i32_16x16x64_i8 v[118:121], v[162:165], v[170:173], v[118:121]
	v_mfma_i32_16x16x64_i8 v[106:109], v[154:157], v[178:181], v[106:109]
	v_mfma_i32_16x16x64_i8 v[102:105], v[162:165], v[178:181], v[102:105]
	v_mfma_i32_16x16x64_i8 v[90:93], v[154:157], v[186:189], v[90:93]
	v_mfma_i32_16x16x64_i8 v[86:89], v[162:165], v[186:189], v[86:89]
	v_mfma_i32_16x16x64_i8 v[74:77], v[154:157], v[194:197], v[74:77]
	v_mfma_i32_16x16x64_i8 v[70:73], v[162:165], v[194:197], v[70:73]
	s_setprio 0
	s_barrier
	s_add_i32 s11, s11, s31
	v_lshl_add_u64 v[206:207], s[4:5], 0, v[198:199]
	s_mov_b32 m0, s11
	ds_read_b128 v[166:169], v217 offset:16384
	ds_read_b128 v[170:173], v217 offset:17408
	ds_read_b128 v[174:177], v217 offset:18432
	ds_read_b128 v[178:181], v217 offset:19456
	ds_read_b128 v[182:185], v217 offset:20480
	ds_read_b128 v[186:189], v217 offset:21504
	ds_read_b128 v[190:193], v217 offset:22528
	ds_read_b128 v[194:197], v217 offset:23552
	global_load_lds_dwordx4 v[206:207], off
	s_add_i32 m0, s11, 0x2000
	s_add_u32 s12, s4, 0x40000
	v_lshl_add_u64 v[208:209], s[4:5], 0, v[200:201]
	s_addc_u32 s13, s5, 0
	s_add_i32 s11, s14, s31
	global_load_lds_dwordx4 v[208:209], off
	v_lshl_add_u64 v[4:5], s[12:13], 0, v[198:199]
	s_mov_b32 m0, s11
	v_lshl_add_u64 v[210:211], s[8:9], 0, v[202:203]
	global_load_lds_dwordx4 v[4:5], off
	v_lshl_add_u64 v[4:5], s[12:13], 0, v[200:201]
	s_add_i32 m0, s11, 0x2000
	v_lshl_add_u64 v[220:221], s[8:9], 0, v[204:205]
	global_load_lds_dwordx4 v[4:5], off
	s_mov_b32 m0, s60
	s_nop 0
	global_load_lds_dwordx4 v[210:211], off
	s_add_i32 m0, s60, 0x2000
	s_nop 0
	global_load_lds_dwordx4 v[220:221], off
	s_waitcnt vmcnt(8)
	s_waitcnt lgkmcnt(0)
	s_barrier
	s_setprio 1
	s_waitcnt lgkmcnt(0)
	v_mfma_i32_16x16x64_i8 v[66:69], v[134:137], v[166:169], 0
	v_mfma_i32_16x16x64_i8 v[62:65], v[142:145], v[166:169], 0
	v_mfma_i32_16x16x64_i8 v[50:53], v[134:137], v[174:177], 0
	v_mfma_i32_16x16x64_i8 v[46:49], v[142:145], v[174:177], 0
	v_mfma_i32_16x16x64_i8 v[34:37], v[134:137], v[182:185], 0
	v_mfma_i32_16x16x64_i8 v[30:33], v[142:145], v[182:185], 0
	v_mfma_i32_16x16x64_i8 v[18:21], v[134:137], v[190:193], 0
	v_mfma_i32_16x16x64_i8 v[14:17], v[142:145], v[190:193], 0
	v_mfma_i32_16x16x64_i8 v[66:69], v[138:141], v[170:173], v[66:69]
	v_mfma_i32_16x16x64_i8 v[62:65], v[146:149], v[170:173], v[62:65]
	v_mfma_i32_16x16x64_i8 v[50:53], v[138:141], v[178:181], v[50:53]
	v_mfma_i32_16x16x64_i8 v[46:49], v[146:149], v[178:181], v[46:49]
	v_mfma_i32_16x16x64_i8 v[34:37], v[138:141], v[186:189], v[34:37]
	v_mfma_i32_16x16x64_i8 v[30:33], v[146:149], v[186:189], v[30:33]
	v_mfma_i32_16x16x64_i8 v[18:21], v[138:141], v[194:197], v[18:21]
	v_mfma_i32_16x16x64_i8 v[14:17], v[146:149], v[194:197], v[14:17]
	s_setprio 0
	s_setprio 1
	v_mfma_i32_16x16x64_i8 v[58:61], v[150:153], v[166:169], 0
	v_mfma_i32_16x16x64_i8 v[54:57], v[158:161], v[166:169], 0
	v_mfma_i32_16x16x64_i8 v[42:45], v[150:153], v[174:177], 0
	v_mfma_i32_16x16x64_i8 v[38:41], v[158:161], v[174:177], 0
	v_mfma_i32_16x16x64_i8 v[26:29], v[150:153], v[182:185], 0
	v_mfma_i32_16x16x64_i8 v[22:25], v[158:161], v[182:185], 0
	v_mfma_i32_16x16x64_i8 v[10:13], v[150:153], v[190:193], 0
	v_mfma_i32_16x16x64_i8 v[4:7], v[158:161], v[190:193], 0
	v_mfma_i32_16x16x64_i8 v[58:61], v[154:157], v[170:173], v[58:61]
	v_mfma_i32_16x16x64_i8 v[54:57], v[162:165], v[170:173], v[54:57]
	v_mfma_i32_16x16x64_i8 v[42:45], v[154:157], v[178:181], v[42:45]
	v_mfma_i32_16x16x64_i8 v[38:41], v[162:165], v[178:181], v[38:41]
	v_mfma_i32_16x16x64_i8 v[26:29], v[154:157], v[186:189], v[26:29]
	v_mfma_i32_16x16x64_i8 v[22:25], v[162:165], v[186:189], v[22:25]
	v_mfma_i32_16x16x64_i8 v[10:13], v[154:157], v[194:197], v[10:13]
	v_mfma_i32_16x16x64_i8 v[4:7], v[162:165], v[194:197], v[4:7]
	s_setprio 0
	s_barrier
	s_add_i32 s11, 0, 0x18000
	v_add_u32_e32 v3, s11, v212
	s_add_i32 s12, 0, 0x1c000
	ds_read_b128 v[134:137], v3
	ds_read_b128 v[138:141], v3 offset:1024
	ds_read_b128 v[142:145], v3 offset:2048
	ds_read_b128 v[146:149], v3 offset:3072
	v_add_u32_e32 v3, s12, v212
	ds_read_b128 v[150:153], v3
	ds_read_b128 v[154:157], v3 offset:1024
	ds_read_b128 v[158:161], v3 offset:2048
	ds_read_b128 v[162:165], v3 offset:3072
	s_add_u32 s8, s8, 0x40000
	s_addc_u32 s9, s9, 0
	v_lshl_add_u64 v[8:9], s[8:9], 0, v[202:203]
	s_add_i32 m0, s60, 0x4000
	ds_read_b128 v[166:169], v217 offset:32768
	ds_read_b128 v[170:173], v217 offset:33792
	ds_read_b128 v[174:177], v217 offset:34816
	ds_read_b128 v[178:181], v217 offset:35840
	ds_read_b128 v[182:185], v217 offset:36864
	ds_read_b128 v[186:189], v217 offset:37888
	ds_read_b128 v[190:193], v217 offset:38912
	ds_read_b128 v[194:197], v217 offset:39936
	global_load_lds_dwordx4 v[8:9], off
	v_lshl_add_u64 v[8:9], s[8:9], 0, v[204:205]
	s_add_i32 m0, s60, 0x6000
	s_nop 0
	global_load_lds_dwordx4 v[8:9], off
	s_waitcnt vmcnt(8)
	s_waitcnt lgkmcnt(0)
	s_barrier
	s_setprio 1
	s_waitcnt lgkmcnt(0)
	v_mfma_i32_16x16x64_i8 v[130:133], v[134:137], v[166:169], v[130:133]
	v_mfma_i32_16x16x64_i8 v[126:129], v[142:145], v[166:169], v[126:129]
	v_mfma_i32_16x16x64_i8 v[114:117], v[134:137], v[174:177], v[114:117]
	v_mfma_i32_16x16x64_i8 v[110:113], v[142:145], v[174:177], v[110:113]
	v_mfma_i32_16x16x64_i8 v[98:101], v[134:137], v[182:185], v[98:101]
	v_mfma_i32_16x16x64_i8 v[94:97], v[142:145], v[182:185], v[94:97]
	v_mfma_i32_16x16x64_i8 v[82:85], v[134:137], v[190:193], v[82:85]
	v_mfma_i32_16x16x64_i8 v[78:81], v[142:145], v[190:193], v[78:81]
	v_mfma_i32_16x16x64_i8 v[130:133], v[138:141], v[170:173], v[130:133]
	v_mfma_i32_16x16x64_i8 v[126:129], v[146:149], v[170:173], v[126:129]
	v_mfma_i32_16x16x64_i8 v[114:117], v[138:141], v[178:181], v[114:117]
	v_mfma_i32_16x16x64_i8 v[110:113], v[146:149], v[178:181], v[110:113]
	v_mfma_i32_16x16x64_i8 v[98:101], v[138:141], v[186:189], v[98:101]
	v_mfma_i32_16x16x64_i8 v[94:97], v[146:149], v[186:189], v[94:97]
	v_mfma_i32_16x16x64_i8 v[82:85], v[138:141], v[194:197], v[82:85]
	v_mfma_i32_16x16x64_i8 v[78:81], v[146:149], v[194:197], v[78:81]
	s_setprio 0
	s_setprio 1
	v_mfma_i32_16x16x64_i8 v[122:125], v[150:153], v[166:169], v[122:125]
	v_mfma_i32_16x16x64_i8 v[118:121], v[158:161], v[166:169], v[118:121]
	v_mfma_i32_16x16x64_i8 v[106:109], v[150:153], v[174:177], v[106:109]
	v_mfma_i32_16x16x64_i8 v[102:105], v[158:161], v[174:177], v[102:105]
	v_mfma_i32_16x16x64_i8 v[90:93], v[150:153], v[182:185], v[90:93]
	v_mfma_i32_16x16x64_i8 v[86:89], v[158:161], v[182:185], v[86:89]
	v_mfma_i32_16x16x64_i8 v[74:77], v[150:153], v[190:193], v[74:77]
	v_mfma_i32_16x16x64_i8 v[70:73], v[158:161], v[190:193], v[70:73]
	v_mfma_i32_16x16x64_i8 v[122:125], v[154:157], v[170:173], v[122:125]
	v_mfma_i32_16x16x64_i8 v[118:121], v[162:165], v[170:173], v[118:121]
	v_mfma_i32_16x16x64_i8 v[106:109], v[154:157], v[178:181], v[106:109]
	v_mfma_i32_16x16x64_i8 v[102:105], v[162:165], v[178:181], v[102:105]
	v_mfma_i32_16x16x64_i8 v[90:93], v[154:157], v[186:189], v[90:93]
	v_mfma_i32_16x16x64_i8 v[86:89], v[162:165], v[186:189], v[86:89]
	v_mfma_i32_16x16x64_i8 v[74:77], v[154:157], v[194:197], v[74:77]
	v_mfma_i32_16x16x64_i8 v[70:73], v[162:165], v[194:197], v[70:73]
	s_setprio 0
	s_barrier
	s_add_i32 s8, s11, s31
	v_lshl_add_u64 v[8:9], v[206:207], 0, s[28:29]
	s_mov_b32 m0, s8
	ds_read_b128 v[166:169], v217 offset:49152
	ds_read_b128 v[170:173], v217 offset:50176
	ds_read_b128 v[174:177], v217 offset:51200
	ds_read_b128 v[178:181], v217 offset:52224
	ds_read_b128 v[182:185], v217 offset:53248
	ds_read_b128 v[186:189], v217 offset:54272
	ds_read_b128 v[190:193], v217 offset:55296
	ds_read_b128 v[194:197], v217 offset:56320
	global_load_lds_dwordx4 v[8:9], off
	s_add_i32 m0, s8, 0x2000
	s_add_u32 s4, s4, 0x40080
	v_lshl_add_u64 v[8:9], v[208:209], 0, s[28:29]
	s_addc_u32 s5, s5, 0
	s_add_i32 s8, s12, s31
	global_load_lds_dwordx4 v[8:9], off
	v_lshl_add_u64 v[8:9], s[4:5], 0, v[198:199]
	s_mov_b32 m0, s8
	s_nop 0
	global_load_lds_dwordx4 v[8:9], off
	v_lshl_add_u64 v[8:9], s[4:5], 0, v[200:201]
	s_add_i32 m0, s8, 0x2000
	s_nop 0
	global_load_lds_dwordx4 v[8:9], off
	v_lshl_add_u64 v[8:9], v[210:211], 0, s[28:29]
	s_add_i32 m0, s60, 0x8000
	s_nop 0
	global_load_lds_dwordx4 v[8:9], off
	v_lshl_add_u64 v[8:9], v[220:221], 0, s[28:29]
	s_add_i32 m0, s60, 0xa000
	s_nop 0
	global_load_lds_dwordx4 v[8:9], off
	s_waitcnt vmcnt(8)
	s_waitcnt lgkmcnt(0)
	s_barrier
	s_setprio 1
	s_waitcnt lgkmcnt(0)
	v_mfma_i32_16x16x64_i8 v[66:69], v[134:137], v[166:169], v[66:69]
	v_mfma_i32_16x16x64_i8 v[62:65], v[142:145], v[166:169], v[62:65]
	v_mfma_i32_16x16x64_i8 v[50:53], v[134:137], v[174:177], v[50:53]
	v_mfma_i32_16x16x64_i8 v[46:49], v[142:145], v[174:177], v[46:49]
	v_mfma_i32_16x16x64_i8 v[34:37], v[134:137], v[182:185], v[34:37]
	v_mfma_i32_16x16x64_i8 v[30:33], v[142:145], v[182:185], v[30:33]
	v_mfma_i32_16x16x64_i8 v[18:21], v[134:137], v[190:193], v[18:21]
	v_mfma_i32_16x16x64_i8 v[14:17], v[142:145], v[190:193], v[14:17]
	v_mfma_i32_16x16x64_i8 v[66:69], v[138:141], v[170:173], v[66:69]
	v_mfma_i32_16x16x64_i8 v[62:65], v[146:149], v[170:173], v[62:65]
	v_mfma_i32_16x16x64_i8 v[50:53], v[138:141], v[178:181], v[50:53]
	v_mfma_i32_16x16x64_i8 v[46:49], v[146:149], v[178:181], v[46:49]
	v_mfma_i32_16x16x64_i8 v[34:37], v[138:141], v[186:189], v[34:37]
	v_mfma_i32_16x16x64_i8 v[30:33], v[146:149], v[186:189], v[30:33]
	v_mfma_i32_16x16x64_i8 v[18:21], v[138:141], v[194:197], v[18:21]
	v_mfma_i32_16x16x64_i8 v[14:17], v[146:149], v[194:197], v[14:17]
	s_setprio 0
	s_setprio 1
	v_mfma_i32_16x16x64_i8 v[58:61], v[150:153], v[166:169], v[58:61]
	v_mfma_i32_16x16x64_i8 v[54:57], v[158:161], v[166:169], v[54:57]
	v_mfma_i32_16x16x64_i8 v[42:45], v[150:153], v[174:177], v[42:45]
	v_mfma_i32_16x16x64_i8 v[38:41], v[158:161], v[174:177], v[38:41]
	v_mfma_i32_16x16x64_i8 v[26:29], v[150:153], v[182:185], v[26:29]
	v_mfma_i32_16x16x64_i8 v[22:25], v[158:161], v[182:185], v[22:25]
	v_mfma_i32_16x16x64_i8 v[8:11], v[150:153], v[190:193], v[10:13]
	v_mfma_i32_16x16x64_i8 v[4:7], v[158:161], v[190:193], v[4:7]
	v_mfma_i32_16x16x64_i8 v[58:61], v[154:157], v[170:173], v[58:61]
	v_mfma_i32_16x16x64_i8 v[54:57], v[162:165], v[170:173], v[54:57]
	v_mfma_i32_16x16x64_i8 v[42:45], v[154:157], v[178:181], v[42:45]
	v_mfma_i32_16x16x64_i8 v[38:41], v[162:165], v[178:181], v[38:41]
	v_mfma_i32_16x16x64_i8 v[26:29], v[154:157], v[186:189], v[26:29]
	v_mfma_i32_16x16x64_i8 v[22:25], v[162:165], v[186:189], v[22:25]
	v_mfma_i32_16x16x64_i8 v[10:13], v[154:157], v[194:197], v[8:11]
	v_mfma_i32_16x16x64_i8 v[6:9], v[162:165], v[194:197], v[4:7]
	s_setprio 0
	s_barrier
	s_add_i32 s10, s10, 2
	s_add_u32 s0, s0, 0x100
	s_addc_u32 s1, s1, 0
	s_add_u32 s37, s37, 0x100
	s_addc_u32 s81, s81, 0
	s_cmp_gt_u32 s10, 13
